# up-projection output: three quarters of H stored with the default cache policy, one quarter nt
# baseline (speedup 1.0000x reference)
; #define PG8_LAS __attribute__((address_space(3)))
; #define PG8_GAS __attribute__((address_space(1)))
; #define PG8_PACK8(y0, y1) (u32x4){cvt_pk_bf16((y0)[0], (y0)[1]), cvt_pk_bf16((y0)[2], (y0)[3]), cvt_pk_bf16((y1)[0], (y1)[1]), cvt_pk_bf16((y1)[2], (y1)[3])}
;     __device__ __forceinline__ void operator()(const f32x4 (&acc)[2][2][4][2], const Unit& u, int ui, int wr, int wc, int fr, int fq) const {
;     ...
;         const unsigned row0 = (unsigned)(u.pm * BM + wr * 64 + fr), colp = (unsigned)((u.pn & 3) * BM + wc * 32 + 8 * fq);
;         const PG8_LAS float* rsp = tab + (u.pm == pmA ? 0 : 256) + wr * 64 + fr;
;         float rsv[2][4];
; #pragma unroll
;         for (int ai = 0; ai < 2; ++ai)
; #pragma unroll
;             for (int m = 0; m < 4; ++m) rsv[ai][m] = rsp[ai * HALF + m * 16];
; #pragma unroll
;         for (int ai = 0; ai < 2; ++ai)
; #pragma unroll
;             for (int m = 0; m < 4; ++m) {
;                 const unsigned row = row0 + ai * HALF + m * 16; const float rs = rsv[ai][m];
; #pragma unroll
;                 for (int bj = 0; bj < 2; ++bj) {
;                     f32x4 y0 = acc[ai][bj][m][0] * rs, y1 = acc[ai][bj][m][1] * rs;
; #pragma unroll
;                     for (int e = 0; e < 4; ++e) { const float a = fmaxf(y0[e], 0.f), b = fmaxf(y1[e], 0.f); y0[e] = a * a; y1[e] = b * b; }
;                     const u32x4 hw = PG8_PACK8(y0, y1);
;     ...
;                     if (probe_mode == 1) { asm volatile("" :: "v"(hw)); } else
;     ...
;                     *(PG8_GAS u32x4*)((PG8_GAS unsigned char*)ws + E_QKVO + (size_t)((unsigned)(u.pm >> 4) * (24u << 20) + (unsigned)(u.pn >> 2) * (8u << 20) + row * 2048u + (colp + bj * HALF) * 2u)) = hw;
;                 }
.LBB0_64:
	s_lshl_b32 s13, s51, 9
	s_cmp_eq_u32 s20, s29
	s_cselect_b32 s15, 0, 0x400
	v_add_u32_e32 v140, s15, v145
	ds_read2_b32 v[164:165], v140 offset1:16
	ds_read2_b32 v[166:167], v140 offset0:32 offset1:48
	ds_read2_b32 v[142:143], v140 offset0:128 offset1:144
	ds_read2_b32 v[140:141], v140 offset0:160 offset1:176
	s_lshl_b32 s22, s51, 21
	s_lshr_b32 s15, s20, 4
	s_and_b32 s22, s22, 0xff800000
	s_lshl_b32 s20, s20, 19
	s_waitcnt lgkmcnt(0)
	v_pk_mul_f32 v[122:123], v[122:123], v[164:165] op_sel_hi:[1,0]
	s_add_i32 s22, s22, s20
	v_pk_mul_f32 v[126:127], v[126:127], v[164:165] op_sel_hi:[1,0]
	v_pk_mul_f32 v[124:125], v[124:125], v[164:165] op_sel_hi:[1,0]
	v_max_f32_e32 v122, 0, v122
	s_and_b32 s13, s13, 0x600
	v_add_u32_e32 v163, s22, v146
	v_pk_mul_f32 v[128:129], v[128:129], v[164:165] op_sel_hi:[1,0]
	v_mul_f32_e32 v168, v122, v122
	v_max_f32_e32 v122, 0, v127
	v_max_f32_e32 v123, 0, v123
	v_max_f32_e32 v124, 0, v124
	s_mul_i32 s15, s15, 0x1800000
	v_or_b32_e32 v163, s13, v163
	v_max_f32_e32 v126, 0, v126
	v_mul_f32_e32 v122, v122, v122
	v_mul_f32_e32 v127, v123, v123
	v_max_f32_e32 v123, 0, v128
	v_mul_f32_e32 v128, v124, v124
	v_max_f32_e32 v124, 0, v129
	v_max_f32_e32 v125, 0, v125
	v_pk_mul_f32 v[114:115], v[114:115], v[164:165] op_sel_hi:[1,0]
	v_add_u32_e32 v163, s15, v163
	v_mul_f32_e32 v126, v126, v126
	v_mul_f32_e32 v123, v123, v123
	v_mul_f32_e32 v124, v124, v124
	v_mul_f32_e32 v125, v125, v125
	v_cvt_pk_bf16_f32 v122, v126, v122
	v_pk_mul_f32 v[120:121], v[120:121], v[164:165] op_sel_hi:[1,0]
	v_pk_mul_f32 v[118:119], v[118:119], v[164:165] op_sel_hi:[1,0]
	v_pk_mul_f32 v[116:117], v[116:117], v[164:165] op_sel_hi:[1,0]
	v_max_f32_e32 v114, 0, v114
	v_max_f32_e32 v115, 0, v115
	v_cvt_pk_bf16_f32 v123, v123, v124
	v_cvt_pk_bf16_f32 v124, v168, v127
	v_cvt_pk_bf16_f32 v125, v128, v125
	global_store_dwordx4 v163, v[122:125], s[10:11] nt
	v_max_f32_e32 v118, 0, v118
	v_max_f32_e32 v116, 0, v116
	v_mul_f32_e32 v122, v114, v114
	v_max_f32_e32 v114, 0, v119
	v_mul_f32_e32 v119, v115, v115
	v_max_f32_e32 v115, 0, v120
	v_mul_f32_e32 v118, v118, v118
	v_mul_f32_e32 v114, v114, v114
	v_mul_f32_e32 v115, v115, v115
	v_mul_f32_e32 v120, v116, v116
	v_max_f32_e32 v116, 0, v121
	v_max_f32_e32 v117, 0, v117
	v_mul_f32_e32 v116, v116, v116
	v_mul_f32_e32 v117, v117, v117
	v_cvt_pk_bf16_f32 v114, v118, v114
	v_cvt_pk_bf16_f32 v115, v115, v116
	v_or_b32_e32 v118, 0x100, v163
	v_cvt_pk_bf16_f32 v116, v122, v119
	v_cvt_pk_bf16_f32 v117, v120, v117
	global_store_dwordx4 v118, v[114:117], s[10:11] nt
	v_pk_mul_f32 v[90:91], v[90:91], v[166:167] op_sel_hi:[1,0]
	v_pk_mul_f32 v[94:95], v[94:95], v[166:167] op_sel_hi:[1,0]
	v_or_b32_e32 v115, 0x8000, v163
	v_mov_b32_e32 v114, v165
	v_pk_mul_f32 v[106:107], v[106:107], v[114:115] op_sel_hi:[1,0]
	v_pk_mul_f32 v[110:111], v[110:111], v[114:115] op_sel_hi:[1,0]
	v_pk_mul_f32 v[108:109], v[108:109], v[114:115] op_sel_hi:[1,0]
	v_max_f32_e32 v106, 0, v106
	v_pk_mul_f32 v[112:113], v[112:113], v[114:115] op_sel_hi:[1,0]
	v_mul_f32_e32 v116, v106, v106
	v_max_f32_e32 v106, 0, v111
	v_max_f32_e32 v107, 0, v107
	v_max_f32_e32 v108, 0, v108
	v_max_f32_e32 v110, 0, v110
	v_mul_f32_e32 v106, v106, v106
	v_mul_f32_e32 v111, v107, v107
	v_max_f32_e32 v107, 0, v112
	v_mul_f32_e32 v112, v108, v108
	v_max_f32_e32 v108, 0, v113
	v_max_f32_e32 v109, 0, v109
	v_pk_mul_f32 v[98:99], v[98:99], v[114:115] op_sel_hi:[1,0]
	v_mul_f32_e32 v110, v110, v110
	v_mul_f32_e32 v107, v107, v107
	v_mul_f32_e32 v108, v108, v108
	v_mul_f32_e32 v109, v109, v109
	v_cvt_pk_bf16_f32 v106, v110, v106
	v_pk_mul_f32 v[104:105], v[104:105], v[114:115] op_sel_hi:[1,0]
	v_pk_mul_f32 v[102:103], v[102:103], v[114:115] op_sel_hi:[1,0]
	v_pk_mul_f32 v[100:101], v[100:101], v[114:115] op_sel_hi:[1,0]
	v_max_f32_e32 v98, 0, v98
	v_max_f32_e32 v99, 0, v99
	v_cvt_pk_bf16_f32 v107, v107, v108
	v_cvt_pk_bf16_f32 v108, v116, v111
	v_cvt_pk_bf16_f32 v109, v112, v109
	global_store_dwordx4 v115, v[106:109], s[10:11] nt
	v_max_f32_e32 v102, 0, v102
	v_max_f32_e32 v100, 0, v100
	v_mul_f32_e32 v106, v98, v98
	v_max_f32_e32 v98, 0, v103
	v_mul_f32_e32 v103, v99, v99
	v_max_f32_e32 v99, 0, v104
	v_mul_f32_e32 v102, v102, v102
	v_mul_f32_e32 v98, v98, v98
	v_mul_f32_e32 v99, v99, v99
	v_mul_f32_e32 v104, v100, v100
	v_max_f32_e32 v100, 0, v105
	v_max_f32_e32 v101, 0, v101
	v_mul_f32_e32 v100, v100, v100
	v_mul_f32_e32 v101, v101, v101
	v_cvt_pk_bf16_f32 v98, v102, v98
	v_cvt_pk_bf16_f32 v99, v99, v100
	v_or_b32_e32 v102, 0x8100, v163
	v_pk_mul_f32 v[92:93], v[92:93], v[166:167] op_sel_hi:[1,0]
	v_max_f32_e32 v90, 0, v90
	v_cvt_pk_bf16_f32 v100, v106, v103
	v_cvt_pk_bf16_f32 v101, v104, v101
	global_store_dwordx4 v102, v[98:101], s[10:11] nt
	v_pk_mul_f32 v[96:97], v[96:97], v[166:167] op_sel_hi:[1,0]
	v_max_f32_e32 v91, 0, v91
	v_mul_f32_e32 v99, v90, v90
	v_max_f32_e32 v90, 0, v95
	v_max_f32_e32 v92, 0, v92
	v_max_f32_e32 v94, 0, v94
	v_mul_f32_e32 v90, v90, v90
	v_mul_f32_e32 v95, v91, v91
	v_max_f32_e32 v91, 0, v96
	v_mul_f32_e32 v96, v92, v92
	v_max_f32_e32 v92, 0, v97
	v_max_f32_e32 v93, 0, v93
	v_pk_mul_f32 v[82:83], v[82:83], v[166:167] op_sel_hi:[1,0]
	v_or_b32_e32 v98, 0x10000, v163
	v_mul_f32_e32 v94, v94, v94
	v_mul_f32_e32 v91, v91, v91
	v_mul_f32_e32 v92, v92, v92
	v_mul_f32_e32 v93, v93, v93
	v_cvt_pk_bf16_f32 v90, v94, v90
	v_pk_mul_f32 v[88:89], v[88:89], v[166:167] op_sel_hi:[1,0]
	v_pk_mul_f32 v[86:87], v[86:87], v[166:167] op_sel_hi:[1,0]
	v_pk_mul_f32 v[84:85], v[84:85], v[166:167] op_sel_hi:[1,0]
	v_max_f32_e32 v82, 0, v82
	v_max_f32_e32 v83, 0, v83
	v_cvt_pk_bf16_f32 v91, v91, v92
	v_cvt_pk_bf16_f32 v92, v99, v95
	v_cvt_pk_bf16_f32 v93, v96, v93
; #define PG8_GAS __attribute__((address_space(1)))
; #define PG8_PACK8(y0, y1) (u32x4){cvt_pk_bf16((y0)[0], (y0)[1]), cvt_pk_bf16((y0)[2], (y0)[3]), cvt_pk_bf16((y1)[0], (y1)[1]), cvt_pk_bf16((y1)[2], (y1)[3])}
;     __device__ __forceinline__ void operator()(const f32x4 (&acc)[2][2][4][2], const Unit& u, int ui, int wr, int wc, int fr, int fq) const {
;     ...
;         for (int ai = 0; ai < 2; ++ai)
; #pragma unroll
;             for (int m = 0; m < 4; ++m) {
;                 const unsigned row = row0 + ai * HALF + m * 16; const float rs = rsv[ai][m];
; #pragma unroll
;                 for (int bj = 0; bj < 2; ++bj) {
;                     f32x4 y0 = acc[ai][bj][m][0] * rs, y1 = acc[ai][bj][m][1] * rs;
; #pragma unroll
;                     for (int e = 0; e < 4; ++e) { const float a = fmaxf(y0[e], 0.f), b = fmaxf(y1[e], 0.f); y0[e] = a * a; y1[e] = b * b; }
;                     const u32x4 hw = PG8_PACK8(y0, y1);
;     ...
;                     if (probe_mode == 1) { asm volatile("" :: "v"(hw)); } else
;     ...
;                     *(PG8_GAS u32x4*)((PG8_GAS unsigned char*)ws + E_QKVO + (size_t)((unsigned)(u.pm >> 4) * (24u << 20) + (unsigned)(u.pn >> 2) * (8u << 20) + row * 2048u + (colp + bj * HALF) * 2u)) = hw;
;                 }
	global_store_dwordx4 v98, v[90:93], s[10:11]
	v_max_f32_e32 v86, 0, v86
	v_max_f32_e32 v84, 0, v84
	v_mul_f32_e32 v90, v82, v82
	v_max_f32_e32 v82, 0, v87
	v_mul_f32_e32 v87, v83, v83
	v_max_f32_e32 v83, 0, v88
	v_mul_f32_e32 v86, v86, v86
	v_mul_f32_e32 v82, v82, v82
	v_mul_f32_e32 v83, v83, v83
	v_mul_f32_e32 v88, v84, v84
	v_max_f32_e32 v84, 0, v89
	v_max_f32_e32 v85, 0, v85
	v_mul_f32_e32 v84, v84, v84
	v_mul_f32_e32 v85, v85, v85
	v_cvt_pk_bf16_f32 v82, v86, v82
	v_cvt_pk_bf16_f32 v83, v83, v84
	v_or_b32_e32 v86, 0x10100, v163
	v_cvt_pk_bf16_f32 v84, v90, v87
	v_cvt_pk_bf16_f32 v85, v88, v85
	global_store_dwordx4 v86, v[82:85], s[10:11]
	v_pk_mul_f32 v[58:59], v[58:59], v[142:143] op_sel_hi:[1,0]
	v_pk_mul_f32 v[62:63], v[62:63], v[142:143] op_sel_hi:[1,0]
	v_or_b32_e32 v83, 0x18000, v163
	v_mov_b32_e32 v82, v167
	v_pk_mul_f32 v[74:75], v[74:75], v[82:83] op_sel_hi:[1,0]
	v_pk_mul_f32 v[78:79], v[78:79], v[82:83] op_sel_hi:[1,0]
	v_pk_mul_f32 v[76:77], v[76:77], v[82:83] op_sel_hi:[1,0]
	v_max_f32_e32 v74, 0, v74
	v_pk_mul_f32 v[80:81], v[80:81], v[82:83] op_sel_hi:[1,0]
	v_mul_f32_e32 v84, v74, v74
	v_max_f32_e32 v74, 0, v79
	v_max_f32_e32 v75, 0, v75
	v_max_f32_e32 v76, 0, v76
	v_max_f32_e32 v78, 0, v78
	v_mul_f32_e32 v74, v74, v74
	v_mul_f32_e32 v79, v75, v75
	v_max_f32_e32 v75, 0, v80
	v_mul_f32_e32 v80, v76, v76
	v_max_f32_e32 v76, 0, v81
	v_max_f32_e32 v77, 0, v77
	v_pk_mul_f32 v[66:67], v[66:67], v[82:83] op_sel_hi:[1,0]
	v_mul_f32_e32 v78, v78, v78
	v_mul_f32_e32 v75, v75, v75
	v_mul_f32_e32 v76, v76, v76
	v_mul_f32_e32 v77, v77, v77
	v_cvt_pk_bf16_f32 v74, v78, v74
	v_pk_mul_f32 v[72:73], v[72:73], v[82:83] op_sel_hi:[1,0]
	v_pk_mul_f32 v[70:71], v[70:71], v[82:83] op_sel_hi:[1,0]
	v_pk_mul_f32 v[68:69], v[68:69], v[82:83] op_sel_hi:[1,0]
	v_max_f32_e32 v66, 0, v66
	v_max_f32_e32 v67, 0, v67
	v_cvt_pk_bf16_f32 v75, v75, v76
	v_cvt_pk_bf16_f32 v76, v84, v79
	v_cvt_pk_bf16_f32 v77, v80, v77
	global_store_dwordx4 v83, v[74:77], s[10:11]
	v_max_f32_e32 v70, 0, v70
	v_max_f32_e32 v68, 0, v68
	v_mul_f32_e32 v74, v66, v66
	v_max_f32_e32 v66, 0, v71
	v_mul_f32_e32 v71, v67, v67
	v_max_f32_e32 v67, 0, v72
	v_mul_f32_e32 v70, v70, v70
	v_mul_f32_e32 v66, v66, v66
	v_mul_f32_e32 v67, v67, v67
	v_mul_f32_e32 v72, v68, v68
	v_max_f32_e32 v68, 0, v73
	v_max_f32_e32 v69, 0, v69
	v_mul_f32_e32 v68, v68, v68
	v_mul_f32_e32 v69, v69, v69
	v_cvt_pk_bf16_f32 v66, v70, v66
	v_cvt_pk_bf16_f32 v67, v67, v68
	v_or_b32_e32 v70, 0x18100, v163
	v_pk_mul_f32 v[60:61], v[60:61], v[142:143] op_sel_hi:[1,0]
	v_max_f32_e32 v58, 0, v58
	v_cvt_pk_bf16_f32 v68, v74, v71
	v_cvt_pk_bf16_f32 v69, v72, v69
	global_store_dwordx4 v70, v[66:69], s[10:11]
	v_pk_mul_f32 v[64:65], v[64:65], v[142:143] op_sel_hi:[1,0]
	v_max_f32_e32 v59, 0, v59
	v_mul_f32_e32 v67, v58, v58
	v_max_f32_e32 v58, 0, v63
	v_max_f32_e32 v60, 0, v60
	v_max_f32_e32 v62, 0, v62
	v_mul_f32_e32 v58, v58, v58
	v_mul_f32_e32 v63, v59, v59
	v_max_f32_e32 v59, 0, v64
	v_mul_f32_e32 v64, v60, v60
	v_max_f32_e32 v60, 0, v65
	v_max_f32_e32 v61, 0, v61
	v_pk_mul_f32 v[50:51], v[50:51], v[142:143] op_sel_hi:[1,0]
	v_add_u32_e32 v66, 0x40000, v163
	v_mul_f32_e32 v62, v62, v62
	v_mul_f32_e32 v59, v59, v59
	v_mul_f32_e32 v60, v60, v60
	v_mul_f32_e32 v61, v61, v61
	v_cvt_pk_bf16_f32 v58, v62, v58
	v_pk_mul_f32 v[56:57], v[56:57], v[142:143] op_sel_hi:[1,0]
	v_pk_mul_f32 v[54:55], v[54:55], v[142:143] op_sel_hi:[1,0]
	v_pk_mul_f32 v[52:53], v[52:53], v[142:143] op_sel_hi:[1,0]
	v_max_f32_e32 v50, 0, v50
	v_max_f32_e32 v51, 0, v51
	v_cvt_pk_bf16_f32 v59, v59, v60
	v_cvt_pk_bf16_f32 v60, v67, v63
	v_cvt_pk_bf16_f32 v61, v64, v61
	global_store_dwordx4 v66, v[58:61], s[10:11]
	v_max_f32_e32 v54, 0, v54
	v_max_f32_e32 v52, 0, v52
	v_mul_f32_e32 v58, v50, v50
	v_max_f32_e32 v50, 0, v55
	v_mul_f32_e32 v55, v51, v51
	v_max_f32_e32 v51, 0, v56
	v_mul_f32_e32 v54, v54, v54
	v_mul_f32_e32 v50, v50, v50
	v_mul_f32_e32 v51, v51, v51
	v_mul_f32_e32 v56, v52, v52
	v_max_f32_e32 v52, 0, v57
	v_max_f32_e32 v53, 0, v53
	v_mul_f32_e32 v52, v52, v52
	v_mul_f32_e32 v53, v53, v53
	v_cvt_pk_bf16_f32 v50, v54, v50
	v_cvt_pk_bf16_f32 v51, v51, v52
	v_add_u32_e32 v54, 0x40100, v163
	v_cvt_pk_bf16_f32 v52, v58, v55
	v_cvt_pk_bf16_f32 v53, v56, v53
	global_store_dwordx4 v54, v[50:53], s[10:11]
	v_pk_mul_f32 v[26:27], v[26:27], v[140:141] op_sel_hi:[1,0]
	v_pk_mul_f32 v[30:31], v[30:31], v[140:141] op_sel_hi:[1,0]
	v_add_u32_e32 v51, 0x48000, v163
	v_mov_b32_e32 v50, v143
	v_pk_mul_f32 v[42:43], v[42:43], v[50:51] op_sel_hi:[1,0]
	v_pk_mul_f32 v[46:47], v[46:47], v[50:51] op_sel_hi:[1,0]
	v_pk_mul_f32 v[44:45], v[44:45], v[50:51] op_sel_hi:[1,0]
	v_max_f32_e32 v42, 0, v42
	v_pk_mul_f32 v[48:49], v[48:49], v[50:51] op_sel_hi:[1,0]
	v_mul_f32_e32 v52, v42, v42
	v_max_f32_e32 v42, 0, v47
	v_max_f32_e32 v43, 0, v43
	v_max_f32_e32 v44, 0, v44
	v_max_f32_e32 v46, 0, v46
	v_mul_f32_e32 v42, v42, v42
	v_mul_f32_e32 v47, v43, v43
; #define PG8_GAS __attribute__((address_space(1)))
; #define PG8_PACK8(y0, y1) (u32x4){cvt_pk_bf16((y0)[0], (y0)[1]), cvt_pk_bf16((y0)[2], (y0)[3]), cvt_pk_bf16((y1)[0], (y1)[1]), cvt_pk_bf16((y1)[2], (y1)[3])}
;     __device__ __forceinline__ void operator()(const f32x4 (&acc)[2][2][4][2], const Unit& u, int ui, int wr, int wc, int fr, int fq) const {
;     ...
;         for (int ai = 0; ai < 2; ++ai)
; #pragma unroll
;             for (int m = 0; m < 4; ++m) {
;                 const unsigned row = row0 + ai * HALF + m * 16; const float rs = rsv[ai][m];
; #pragma unroll
;                 for (int bj = 0; bj < 2; ++bj) {
;                     f32x4 y0 = acc[ai][bj][m][0] * rs, y1 = acc[ai][bj][m][1] * rs;
; #pragma unroll
;                     for (int e = 0; e < 4; ++e) { const float a = fmaxf(y0[e], 0.f), b = fmaxf(y1[e], 0.f); y0[e] = a * a; y1[e] = b * b; }
;                     const u32x4 hw = PG8_PACK8(y0, y1);
;     ...
;                     if (probe_mode == 1) { asm volatile("" :: "v"(hw)); } else
;     ...
;                     *(PG8_GAS u32x4*)((PG8_GAS unsigned char*)ws + E_QKVO + (size_t)((unsigned)(u.pm >> 4) * (24u << 20) + (unsigned)(u.pn >> 2) * (8u << 20) + row * 2048u + (colp + bj * HALF) * 2u)) = hw;
;                 }
	v_max_f32_e32 v43, 0, v48
	v_mul_f32_e32 v48, v44, v44
	v_max_f32_e32 v44, 0, v49
	v_max_f32_e32 v45, 0, v45
	v_pk_mul_f32 v[34:35], v[34:35], v[50:51] op_sel_hi:[1,0]
	v_mul_f32_e32 v46, v46, v46
	v_mul_f32_e32 v43, v43, v43
	v_mul_f32_e32 v44, v44, v44
	v_mul_f32_e32 v45, v45, v45
	v_cvt_pk_bf16_f32 v42, v46, v42
	v_pk_mul_f32 v[40:41], v[40:41], v[50:51] op_sel_hi:[1,0]
	v_pk_mul_f32 v[38:39], v[38:39], v[50:51] op_sel_hi:[1,0]
	v_pk_mul_f32 v[36:37], v[36:37], v[50:51] op_sel_hi:[1,0]
	v_max_f32_e32 v34, 0, v34
	v_max_f32_e32 v35, 0, v35
	v_cvt_pk_bf16_f32 v43, v43, v44
	v_cvt_pk_bf16_f32 v44, v52, v47
	v_cvt_pk_bf16_f32 v45, v48, v45
	global_store_dwordx4 v51, v[42:45], s[10:11]
	v_max_f32_e32 v38, 0, v38
	v_max_f32_e32 v36, 0, v36
	v_mul_f32_e32 v42, v34, v34
	v_max_f32_e32 v34, 0, v39
	v_mul_f32_e32 v39, v35, v35
	v_max_f32_e32 v35, 0, v40
	v_mul_f32_e32 v38, v38, v38
	v_mul_f32_e32 v34, v34, v34
	v_mul_f32_e32 v35, v35, v35
	v_mul_f32_e32 v40, v36, v36
	v_max_f32_e32 v36, 0, v41
	v_max_f32_e32 v37, 0, v37
	v_mul_f32_e32 v36, v36, v36
	v_mul_f32_e32 v37, v37, v37
	v_cvt_pk_bf16_f32 v34, v38, v34
	v_cvt_pk_bf16_f32 v35, v35, v36
	v_add_u32_e32 v38, 0x48100, v163
	v_pk_mul_f32 v[28:29], v[28:29], v[140:141] op_sel_hi:[1,0]
	v_max_f32_e32 v26, 0, v26
	v_cvt_pk_bf16_f32 v36, v42, v39
	v_cvt_pk_bf16_f32 v37, v40, v37
	global_store_dwordx4 v38, v[34:37], s[10:11]
	v_pk_mul_f32 v[32:33], v[32:33], v[140:141] op_sel_hi:[1,0]
	v_max_f32_e32 v27, 0, v27
	v_mul_f32_e32 v35, v26, v26
	v_max_f32_e32 v26, 0, v31
	v_max_f32_e32 v28, 0, v28
	v_max_f32_e32 v30, 0, v30
	v_mul_f32_e32 v26, v26, v26
	v_mul_f32_e32 v31, v27, v27
	v_max_f32_e32 v27, 0, v32
	v_mul_f32_e32 v32, v28, v28
	v_max_f32_e32 v28, 0, v33
	v_max_f32_e32 v29, 0, v29
	v_pk_mul_f32 v[18:19], v[18:19], v[140:141] op_sel_hi:[1,0]
	v_add_u32_e32 v34, 0x50000, v163
	v_mul_f32_e32 v30, v30, v30
	v_mul_f32_e32 v27, v27, v27
	v_mul_f32_e32 v28, v28, v28
	v_mul_f32_e32 v29, v29, v29
	v_cvt_pk_bf16_f32 v26, v30, v26
	v_pk_mul_f32 v[24:25], v[24:25], v[140:141] op_sel_hi:[1,0]
	v_pk_mul_f32 v[22:23], v[22:23], v[140:141] op_sel_hi:[1,0]
	v_pk_mul_f32 v[20:21], v[20:21], v[140:141] op_sel_hi:[1,0]
	v_max_f32_e32 v18, 0, v18
	v_max_f32_e32 v19, 0, v19
	v_cvt_pk_bf16_f32 v27, v27, v28
	v_cvt_pk_bf16_f32 v28, v35, v31
	v_cvt_pk_bf16_f32 v29, v32, v29
	global_store_dwordx4 v34, v[26:29], s[10:11]
	v_max_f32_e32 v22, 0, v22
	v_max_f32_e32 v20, 0, v20
	v_mul_f32_e32 v26, v18, v18
	v_max_f32_e32 v18, 0, v23
	v_mul_f32_e32 v23, v19, v19
	v_max_f32_e32 v19, 0, v24
	v_mul_f32_e32 v22, v22, v22
	v_mul_f32_e32 v18, v18, v18
	v_mul_f32_e32 v19, v19, v19
	v_mul_f32_e32 v24, v20, v20
	v_max_f32_e32 v20, 0, v25
	v_max_f32_e32 v21, 0, v21
	v_mul_f32_e32 v20, v20, v20
	v_mul_f32_e32 v21, v21, v21
	v_cvt_pk_bf16_f32 v18, v22, v18
	v_cvt_pk_bf16_f32 v19, v19, v20
	v_add_u32_e32 v22, 0x50100, v163
	v_cvt_pk_bf16_f32 v20, v26, v23
	v_cvt_pk_bf16_f32 v21, v24, v21
	global_store_dwordx4 v22, v[18:21], s[10:11]
	s_andn2_b64 vcc, exec, s[0:1]
	s_mov_b64 s[0:1], -1
	v_add_u32_e32 v19, 0x58000, v163
	v_mov_b32_e32 v18, v141
	v_pk_mul_f32 v[10:11], v[10:11], v[18:19] op_sel_hi:[1,0]
	v_pk_mul_f32 v[14:15], v[14:15], v[18:19] op_sel_hi:[1,0]
	v_pk_mul_f32 v[12:13], v[12:13], v[18:19] op_sel_hi:[1,0]
	v_max_f32_e32 v10, 0, v10
	v_pk_mul_f32 v[16:17], v[16:17], v[18:19] op_sel_hi:[1,0]
	v_mul_f32_e32 v20, v10, v10
	v_max_f32_e32 v10, 0, v15
	v_max_f32_e32 v11, 0, v11
	v_max_f32_e32 v12, 0, v12
	v_max_f32_e32 v14, 0, v14
	v_mul_f32_e32 v10, v10, v10
	v_mul_f32_e32 v15, v11, v11
	v_max_f32_e32 v11, 0, v16
	v_mul_f32_e32 v16, v12, v12
	v_max_f32_e32 v12, 0, v17
	v_max_f32_e32 v13, 0, v13
	v_pk_mul_f32 v[2:3], v[2:3], v[18:19] op_sel_hi:[1,0]
	v_mul_f32_e32 v14, v14, v14
	v_mul_f32_e32 v11, v11, v11
	v_mul_f32_e32 v12, v12, v12
	v_mul_f32_e32 v13, v13, v13
	v_cvt_pk_bf16_f32 v10, v14, v10
	v_pk_mul_f32 v[6:7], v[6:7], v[18:19] op_sel_hi:[1,0]
	v_pk_mul_f32 v[4:5], v[4:5], v[18:19] op_sel_hi:[1,0]
	v_max_f32_e32 v2, 0, v2
	v_cvt_pk_bf16_f32 v11, v11, v12
	v_cvt_pk_bf16_f32 v12, v20, v15
	v_cvt_pk_bf16_f32 v13, v16, v13
	global_store_dwordx4 v19, v[10:13], s[10:11]
	v_pk_mul_f32 v[8:9], v[8:9], v[18:19] op_sel_hi:[1,0]
	v_max_f32_e32 v6, 0, v6
	v_mul_f32_e32 v10, v2, v2
	v_max_f32_e32 v2, 0, v7
	v_max_f32_e32 v3, 0, v3
	v_max_f32_e32 v4, 0, v4
	v_mul_f32_e32 v6, v6, v6
	v_mul_f32_e32 v2, v2, v2
	v_mul_f32_e32 v7, v3, v3
	v_max_f32_e32 v3, 0, v8
	v_mul_f32_e32 v8, v4, v4
	v_max_f32_e32 v4, 0, v9
	v_max_f32_e32 v5, 0, v5
	v_mul_f32_e32 v3, v3, v3
	v_mul_f32_e32 v4, v4, v4
	v_mul_f32_e32 v5, v5, v5
	v_cvt_pk_bf16_f32 v2, v6, v2
	v_add_u32_e32 v6, 0x58100, v163
	v_cvt_pk_bf16_f32 v3, v3, v4
	v_cvt_pk_bf16_f32 v4, v10, v7
	v_cvt_pk_bf16_f32 v5, v8, v5
	global_store_dwordx4 v6, v[2:5], s[10:11]
	s_mov_b32 s100, 2
	s_cbranch_vccnz .LBB0_53
	s_andn2_b64 vcc, exec, s[6:7]
	s_cbranch_vccnz .LBB0_52
	s_barrier
	s_branch .LBB0_52
